# static s_setprio 1 for waves 4-7 for the WHOLE kernel (set once at entry), every other setprio deleted
# speedup vs baseline: 1.0209x; 1.0020x over previous
; #define LAS __attribute__((address_space(3)))
; __device__ __forceinline__ unsigned xb_add(unsigned* p, unsigned v) { return __hip_atomic_fetch_add(p, v, __ATOMIC_RELAXED, __HIP_MEMORY_SCOPE_AGENT); }
; __device__ __forceinline__ unsigned xb_xcc_id() { return (unsigned)__builtin_amdgcn_s_getreg((3 << 11) | 20) & 0xFu; }
; __device__ __forceinline__ XcdBarrier xcd_barrier_post(unsigned* bar, volatile LAS unsigned* st) {
;     XcdBarrier b; b.bar = bar; b.x = xb_xcc_id(); b.st = st;
;     if (threadIdx.x == 0) (void)xb_add(&bar[XB_XCNT(b.x)], 1u);
;     return b;
; __global__ __launch_bounds__(NTHR, 2) void k_mega(Params p) {
;     LAS unsigned char* lds = (LAS unsigned char*)dynlds; LAS unsigned char* xl = lds + XL_OFF;
;     const int G = gridDim.x, c = blockIdx.x;
;     volatile LAS unsigned* xbw = (volatile LAS unsigned*)(lds + LDS_BYTES - 16);
;     if (threadIdx.x == 0) { xbw[0] = 0u; xbw[1] = 0u; xbw[2] = 0u; xbw[3] = 0u; }
;     __syncthreads();
;     const XcdBarrier bar = xcd_barrier_post((unsigned*)(p.ws + WS_CTL), xbw);
.LBB0_2:
	s_or_b64 exec, exec, s[6:7]
	s_load_dwordx2 s[24:25], s[70:71], 0xd8
	s_waitcnt lgkmcnt(0)
	s_barrier
	v_readfirstlane_b32 s98, v0
	s_nop 3
	s_lshr_b32 s98, s98, 8
	s_cmp_lg_u32 s98, 1
	s_cbranch_scc1 .Lprio_done
	s_setprio 1
.Lprio_done:
	s_getreg_b32 s0, hwreg(HW_REG_XCC_ID, 0, 4)
	s_and_b32 s95, s0, 15
	s_mov_b64 s[6:7], exec
	v_readlane_b32 s0, v240, 0
	v_readlane_b32 s1, v240, 1
	s_and_b64 s[0:1], s[6:7], s[0:1]
	s_mov_b64 exec, s[0:1]
	s_cbranch_execz .LBB0_5
	s_mov_b64 s[8:9], exec
	v_mbcnt_lo_u32_b32 v1, s8, 0
	v_mbcnt_hi_u32_b32 v1, s9, v1
	v_cmp_eq_u32_e32 vcc, 0, v1
	s_and_b64 s[0:1], exec, vcc
	s_mov_b64 exec, s[0:1]
	s_cbranch_execz .LBB0_5
	s_lshl_b32 s0, s95, 8
	s_bcnt1_i32_b64 s1, s[8:9]
	v_mov_b32_e32 v1, s0
	v_mov_b32_e32 v2, s1
	global_atomic_add v1, v2, s[24:25] offset:1024

; #define LAS __attribute__((address_space(3)))
; __device__ __forceinline__ unsigned cvt_pk_bf16(float lo, float hi) { const f32x2 v = {lo, hi}; return __builtin_bit_cast(unsigned, __builtin_convertvector(v, bf16x2_t)); }
; #define PG8_WAIT_V(n) asm volatile("s_waitcnt vmcnt(" #n ")" ::: "memory")
; #define PG8_BAR __builtin_amdgcn_s_barrier()
; template <class Epi, class Sched, bool GATHER, bool LIGHTSKIP = false>
; __device__ __forceinline__ void gemm_phase(LAS unsigned char* lds, LAS unsigned char* xl, const int lda, const int ldb, const int K, const Sched& S, const Epi& E) {
;     ...
;     PG8_WAIT_V(0);
;     PG8_BAR;
;     __device__ __forceinline__ void operator()(Acc& acc, const GUnit& u, int wr, int wc, int fr, int fq, LAS unsigned char*, int, int) const {
;         const int row0 = u.x0 + wr * 64 + fr, col0 = u.x1 + wc * 32 + 8 * fq;
; #pragma unroll
;         for (int ai = 0; ai < 2; ++ai)
; #pragma unroll
;             for (int m = 0; m < 4; ++m) { bf16_t* rowp = O + (size_t)(row0 + ai * HALF + m * 16) * ldc + col0;
; #pragma unroll
;                 for (int bj = 0; bj < 2; ++bj) { const f32x4 v0 = acc[ai][bj][m][0], v1 = acc[ai][bj][m][1];
;                     u32x4 w; w.x = cvt_pk_bf16(v0[0], v0[1]); w.y = cvt_pk_bf16(v0[2], v0[3]); w.z = cvt_pk_bf16(v1[0], v1[1]); w.w = cvt_pk_bf16(v1[2], v1[3]);
;                     if constexpr (NT) __builtin_nontemporal_store(w, (u32x4*)(rowp + bj * HALF)); else *(u32x4*)(rowp + bj * HALF) = w; } }
.LBB0_463:
	s_lshr_b32 s2, s92, 3
	s_and_b32 s3, s92, 7
	s_add_u32 s8, s8, 0x44650000
	s_addc_u32 s9, s9, 0
	s_and_b64 s[10:11], s[10:11], exec
	s_cselect_b32 s7, 0x100, 0
	v_add_u32_e32 v132, s7, v1
	v_lshl_or_b32 v1, s6, 8, v142
	v_ashrrev_i32_e32 v133, 31, v132
	v_or_b32_e32 v1, s30, v1
	v_lshlrev_b64 v[130:131], 12, v[132:133]
	v_lshl_add_u64 v[134:135], s[8:9], 0, v[130:131]
	v_lshlrev_b32_e32 v130, 1, v1
	v_mov_b32_e32 v131, 0
	v_lshl_add_u64 v[134:135], v[134:135], 0, v[130:131]
	s_mov_b64 s[6:7], 0x80000
	v_cvt_pk_bf16_f32 v70, v70, v71
	v_cvt_pk_bf16_f32 v71, v72, v73
	v_cvt_pk_bf16_f32 v72, v66, v67
	v_lshl_add_u64 v[66:67], v[134:135], 0, s[6:7]
	s_mov_b32 s6, 0x80000
	v_cvt_pk_bf16_f32 v62, v62, v63
	v_cvt_pk_bf16_f32 v63, v64, v65
	v_cvt_pk_bf16_f32 v64, v58, v59
	v_add_co_u32_e32 v58, vcc, s6, v134
	v_cvt_pk_bf16_f32 v46, v46, v47
	v_cvt_pk_bf16_f32 v47, v48, v49
	v_cvt_pk_bf16_f32 v48, v42, v43
	v_cvt_pk_bf16_f32 v49, v44, v45
	s_mov_b64 s[6:7], 0x90000
	v_cvt_pk_bf16_f32 v110, v110, v111
	v_cvt_pk_bf16_f32 v111, v112, v113
	v_cvt_pk_bf16_f32 v112, v106, v107
	v_or_b32_e32 v106, 16, v132
	v_addc_co_u32_e32 v59, vcc, 0, v135, vcc
	global_store_dwordx4 v[66:67], v[46:49], off offset:256
	v_ashrrev_i32_e32 v107, 31, v106
	v_cvt_pk_bf16_f32 v94, v94, v95
	v_lshl_add_u64 v[46:47], v[134:135], 0, s[6:7]
	s_mov_b32 s6, 0x90000
	v_cvt_pk_bf16_f32 v95, v96, v97
	v_cvt_pk_bf16_f32 v96, v90, v91
	v_or_b32_e32 v90, 32, v132
	v_add_co_u32_e32 v48, vcc, s6, v134
	v_cvt_pk_bf16_f32 v30, v30, v31
	v_cvt_pk_bf16_f32 v31, v32, v33
	v_cvt_pk_bf16_f32 v32, v26, v27
	v_cvt_pk_bf16_f32 v33, v28, v29
	s_mov_b64 s[6:7], 0xa0000
	v_lshlrev_b64 v[106:107], 12, v[106:107]
	v_ashrrev_i32_e32 v91, 31, v90
	v_cvt_pk_bf16_f32 v78, v78, v79
	v_cvt_pk_bf16_f32 v79, v80, v81
	v_cvt_pk_bf16_f32 v80, v74, v75
	v_or_b32_e32 v74, 48, v132
	v_addc_co_u32_e32 v49, vcc, 0, v135, vcc
	global_store_dwordx4 v[46:47], v[30:33], off offset:256
	v_cvt_pk_bf16_f32 v113, v108, v109
	v_lshl_add_u64 v[106:107], s[8:9], 0, v[106:107]
	v_lshl_add_u64 v[30:31], v[134:135], 0, s[6:7]
	s_mov_b32 s6, 0xa0000
	v_lshlrev_b64 v[90:91], 12, v[90:91]
	v_ashrrev_i32_e32 v75, 31, v74
	v_add_co_u32_e32 v32, vcc, s6, v134
	v_cvt_pk_bf16_f32 v14, v14, v15
	v_cvt_pk_bf16_f32 v15, v16, v17
	v_cvt_pk_bf16_f32 v16, v10, v11
	v_cvt_pk_bf16_f32 v17, v12, v13
	s_mov_b64 s[6:7], 0xb0000
	global_store_dwordx4 v[134:135], v[110:113], off offset:256
	v_cvt_pk_bf16_f32 v97, v92, v93
	v_lshl_add_u64 v[90:91], s[8:9], 0, v[90:91]
	v_lshl_add_u64 v[110:111], v[106:107], 0, v[130:131]
	v_lshlrev_b64 v[74:75], 12, v[74:75]
	v_addc_co_u32_e32 v33, vcc, 0, v135, vcc
	global_store_dwordx4 v[30:31], v[14:17], off offset:256
	global_store_dwordx4 v[110:111], v[94:97], off offset:256
	v_cvt_pk_bf16_f32 v81, v76, v77
	v_lshl_add_u64 v[14:15], v[134:135], 0, s[6:7]
	s_mov_b32 s6, 0xb0000
	v_lshl_add_u64 v[94:95], v[90:91], 0, v[130:131]
	v_lshl_add_u64 v[74:75], s[8:9], 0, v[74:75]
	v_add_co_u32_e32 v16, vcc, s6, v134
	v_cvt_pk_bf16_f32 v126, v126, v127
	v_cvt_pk_bf16_f32 v127, v128, v129
	v_cvt_pk_bf16_f32 v128, v122, v123
	v_cvt_pk_bf16_f32 v129, v124, v125
	v_cvt_pk_bf16_f32 v106, v118, v119
	v_cvt_pk_bf16_f32 v107, v120, v121
	v_cvt_pk_bf16_f32 v108, v114, v115
	v_cvt_pk_bf16_f32 v109, v116, v117
	v_cvt_pk_bf16_f32 v90, v102, v103
	v_cvt_pk_bf16_f32 v91, v104, v105
	v_cvt_pk_bf16_f32 v92, v98, v99
	v_cvt_pk_bf16_f32 v93, v100, v101
	global_store_dwordx4 v[94:95], v[78:81], off offset:256
	v_cvt_pk_bf16_f32 v76, v82, v83
	v_cvt_pk_bf16_f32 v77, v84, v85
	v_lshl_add_u64 v[78:79], v[74:75], 0, v[130:131]
	v_cvt_pk_bf16_f32 v74, v86, v87
	v_cvt_pk_bf16_f32 v75, v88, v89
	v_cvt_pk_bf16_f32 v73, v68, v69
	v_cvt_pk_bf16_f32 v65, v60, v61
	v_cvt_pk_bf16_f32 v42, v54, v55
	v_cvt_pk_bf16_f32 v43, v56, v57
	v_cvt_pk_bf16_f32 v44, v50, v51
	v_cvt_pk_bf16_f32 v45, v52, v53
	v_cvt_pk_bf16_f32 v26, v38, v39
	v_cvt_pk_bf16_f32 v27, v40, v41
	v_cvt_pk_bf16_f32 v28, v34, v35
	v_cvt_pk_bf16_f32 v29, v36, v37
	v_cvt_pk_bf16_f32 v10, v22, v23
	v_cvt_pk_bf16_f32 v11, v24, v25
	v_cvt_pk_bf16_f32 v12, v18, v19
	v_cvt_pk_bf16_f32 v13, v20, v21
	v_addc_co_u32_e32 v17, vcc, 0, v135, vcc
	v_cvt_pk_bf16_f32 v6, v6, v7
	v_cvt_pk_bf16_f32 v7, v8, v9
	v_cvt_pk_bf16_f32 v8, v2, v3
	v_cvt_pk_bf16_f32 v9, v4, v5
	global_store_dwordx4 v[134:135], v[126:129], off
	global_store_dwordx4 v[110:111], v[106:109], off
	global_store_dwordx4 v[94:95], v[90:93], off
	global_store_dwordx4 v[78:79], v[74:77], off
	global_store_dwordx4 v[78:79], v[70:73], off offset:256
	global_store_dwordx4 v[58:59], v[62:65], off
	global_store_dwordx4 v[48:49], v[42:45], off
	global_store_dwordx4 v[32:33], v[26:29], off
	global_store_dwordx4 v[16:17], v[10:13], off
	global_store_dwordx4 v[14:15], v[6:9], off offset:256
	v_mov_b32_e32 v15, v0
	s_waitcnt vmcnt(0)
	s_barrier
; __device__ __forceinline__ int otid() { int t = threadIdx.x; asm volatile("" : "+v"(t)); return t; }
; #define PG8_STAGE_B(b, h, bp) PG8_STAGE2(PG8_SB(b, h), (bp) + (h) * hstepB, voffB[0], voffB[1])
; #define PG8_STAGE_A(b, h, ap, NX) do { if constexpr (GATHER) { const unsigned _o0 = (NX) ? vn[h][0] : vc[h][0], _o1 = (NX) ? vn[h][1] : vc[h][1]; PG8_STAGE2(PG8_SA(b, h), (ap), _o0, _o1); } \
;         else { PG8_STAGE2(PG8_SA(b, h), (ap) + (h) * hstepA, voffA[0], voffA[1]); } } while (0)
; #define PG8_BAR __builtin_amdgcn_s_barrier()
; template <class Epi, class Sched, bool GATHER, bool LIGHTSKIP = false>
; __device__ __forceinline__ void gemm_phase(LAS unsigned char* lds, LAS unsigned char* xl, const int lda, const int ldb, const int K, const Sched& S, const Epi& E) {
;     const int tid = otid(), wid = __builtin_amdgcn_readfirstlane(tid >> 6), lane = tid & 63, wr = wid >> 2, wc = wid & 3, fr = lane & 15, fq = lane >> 4;
;     const int nt = K / BK;
;     int Rr[2], Cc[2]; unsigned voffA[2], voffB[2];
; #pragma unroll
;     for (int i = 0; i < 2; ++i) { stage_rc(tid * 16 + i * 8192, Rr[i], Cc[i]); const int Rb = Epi::PERM ? ((Rr[i] & ~31) + perm32(Rr[i] & 31)) : Rr[i];
;         voffA[i] = (unsigned)(Rr[i] * lda + Cc[i]) * 2u; voffB[i] = (unsigned)(Rb * ldb + Cc[i]) * 2u; }
;     unsigned vc[2][2], vn[2][2];
;     const size_t kstep = (size_t)(BK * 2);
;     const size_t hstepA = (size_t)HALF * lda * 2, hstepB = (size_t)HALF * ldb * 2;
;     const unsigned ldsw = (unsigned)wid * 1024u;
;     const int aoff = lds_byte(wr * 64 + fr, fq * 8), boff = lds_byte(wc * 32 + fr, fq * 8);
;     ...
;     GUnit cur, nxt; int ui = 0;
;     if (!S.next(0, cur)) return;
;     Acc acc;
; #pragma unroll
;     for (int a = 0; a < 2; ++a)
; #pragma unroll
;         for (int b = 0; b < 2; ++b)
; #pragma unroll
;             for (int m = 0; m < 4; ++m)
; #pragma unroll
;                 for (int n = 0; n < 2; ++n) acc[a][b][m][n] = (f32x4){0.f, 0.f, 0.f, 0.f};
;     bf16x8 At[4][2], B0[2][2], B1[2][2];
;     const char* cA = cur.A; const char* cB = cur.B;
;     if constexpr (GATHER) { S.offsets(cur, lda, vc);
; #pragma unroll
;         for (int h = 0; h < 2; ++h) { vn[h][0] = vc[h][0]; vn[h][1] = vc[h][1]; } }
;     PG8_STAGE_B(0, 0, cB); PG8_STAGE_B(0, 1, cB); PG8_STAGE_A(0, 0, cA, false); PG8_STAGE_A(0, 1, cA, false);
;     if (wr == 1) PG8_BAR;
;     PG8_WAIT_V(2); PG8_BAR;
	s_load_dwordx2 s[8:9], s[70:71], 0xd8
	s_mov_b32 s7, 0xfffe0
	v_ashrrev_i32_e32 v2, 31, v15
	v_lshrrev_b32_e32 v2, 26, v2
	v_add_u32_e32 v2, v15, v2
	v_ashrrev_i32_e32 v10, 6, v2
	v_bfe_i32 v2, v15, 27, 1
	v_lshlrev_b32_e32 v1, 4, v15
	v_lshrrev_b32_e32 v2, 22, v2
	v_add_u32_e32 v2, v1, v2
	v_and_b32_e32 v2, 0xfffffc00, v2
	v_sub_u32_e32 v2, v1, v2
	v_lshrrev_b32_e32 v3, 4, v2
	v_bitop3_b32 v3, v3, v2, 32 bitop3:0x6c
	v_ashrrev_i32_e32 v2, 31, v2
	v_lshrrev_b32_e32 v2, 26, v2
	v_add_u32_e32 v2, v3, v2
	v_ashrrev_i32_e32 v11, 6, v2
	v_lshlrev_b32_e32 v4, 3, v10
	v_mul_i32_i24_e32 v5, 64, v11
	v_and_b32_e32 v4, -16, v4
	v_sub_u32_e32 v3, v3, v5
	v_mov_b32_e32 v5, 1
	v_add_u32_e32 v2, v11, v4
	v_lshlrev_b32_e32 v4, 5, v10
	v_ashrrev_i16_sdwa v3, v5, sext(v3) dst_sel:DWORD dst_unused:UNUSED_PAD src0_sel:DWORD src1_sel:BYTE_0
	v_and_b32_e32 v4, 32, v4
	v_bfe_i32 v12, v3, 0, 16
	v_and_b32_e32 v7, 3, v11
	v_add_lshl_u32 v4, v4, v12, 1
	v_add_u32_e32 v1, 0x2000, v1
	v_lshlrev_b32_e32 v3, 1, v2
	v_lshrrev_b32_e32 v6, 2, v2
	v_and_or_b32 v7, v2, s7, v7
	v_lshl_add_u32 v132, v2, 12, v4
	v_ashrrev_i32_e32 v2, 31, v1
	v_lshrrev_b32_e32 v2, 22, v2
	v_add_u32_e32 v2, v1, v2
	v_ashrrev_i32_e32 v13, 10, v2
	v_readfirstlane_b32 s6, v15
	v_mul_i32_i24_e32 v2, 0x400, v13
	v_sub_u32_e32 v1, v1, v2
	s_ashr_i32 s15, s6, 6
	s_ashr_i32 s14, s6, 8
	v_and_b32_e32 v3, 24, v3
	v_and_b32_e32 v6, 4, v6
	v_lshrrev_b32_e32 v2, 4, v1
	s_lshl_b32 s20, s15, 10
	s_lshl_b32 s16, s2, 20
	v_or3_b32 v3, v7, v6, v3
	v_bitop3_b32 v1, v2, v1, 32 bitop3:0x6c
	s_waitcnt lgkmcnt(0)
	s_add_u32 s17, s8, s16
	v_lshl_add_u32 v130, v3, 12, v4
	v_ashrrev_i32_e32 v3, 31, v1
	s_addc_u32 s19, s9, 0
	v_lshrrev_b32_e32 v3, 26, v3
	s_add_u32 s10, s17, 0x44450000
	v_add_u32_e32 v3, v1, v3
	s_addc_u32 s11, s19, 0
	s_lshl_b32 s18, s3, 20
	v_lshlrev_b32_e32 v2, 3, v13
	v_ashrrev_i32_e32 v14, 6, v3
	v_and_b32_e32 v3, 0xc0, v3
	s_add_u32 s21, s8, s18
	v_and_b32_e32 v2, -16, v2
	v_sub_u32_e32 v1, v1, v3
	s_addc_u32 s23, s9, 0
	v_add_u32_e32 v2, v14, v2
	v_ashrrev_i16_sdwa v1, v5, sext(v1) dst_sel:DWORD dst_unused:UNUSED_PAD src0_sel:DWORD src1_sel:BYTE_0
	v_and_b32_e32 v5, 3, v14
	s_add_u32 s12, s21, 0x3010000
	v_lshlrev_b32_e32 v4, 5, v13
	v_bfe_i32 v16, v1, 0, 16
	v_lshlrev_b32_e32 v1, 1, v2
	v_lshrrev_b32_e32 v3, 2, v2
	v_and_or_b32 v5, v2, s7, v5
	s_addc_u32 s13, s23, 0
	s_add_i32 s7, s20, 0
	v_and_b32_e32 v4, 32, v4
	v_and_b32_e32 v1, 24, v1
	v_and_b32_e32 v3, 4, v3
	s_add_i32 m0, s7, 0x10000
	v_or3_b32 v1, v5, v3, v1
	v_add_lshl_u32 v3, v4, v16, 1
	global_load_lds_dwordx4 v130, s[12:13]
	s_add_i32 m0, s7, 0x12000
	v_lshl_add_u32 v136, v1, 12, v3
	s_add_u32 s22, s21, 0x3090000
	global_load_lds_dwordx4 v136, s[12:13]
	s_addc_u32 s23, s23, 0
	s_add_i32 m0, s7, 0x14000
	s_add_i32 s26, s7, 0x2000
	global_load_lds_dwordx4 v130, s[22:23]
	s_add_i32 m0, s7, 0x16000
	v_lshl_add_u32 v134, v2, 12, v3
	global_load_lds_dwordx4 v136, s[22:23]
	s_mov_b32 m0, s7
	s_add_u32 s22, s17, 0x444d0000
	global_load_lds_dwordx4 v132, s[10:11]
	s_mov_b32 m0, s26
	s_addc_u32 s23, s19, 0
	s_add_i32 s27, s7, 0x4000
	global_load_lds_dwordx4 v134, s[10:11]
	s_mov_b32 m0, s27
	s_add_i32 s28, s7, 0x6000
	global_load_lds_dwordx4 v132, s[22:23]
	s_mov_b32 m0, s28
	v_mov_b32_e32 v137, v131
	global_load_lds_dwordx4 v134, s[22:23]
	v_mov_b32_e32 v133, v131
	v_mov_b32_e32 v135, v131
	v_lshl_add_u64 v[8:9], s[12:13], 0, v[130:131]
	v_lshl_add_u64 v[6:7], s[12:13], 0, v[136:137]
	v_lshl_add_u64 v[4:5], s[10:11], 0, v[132:133]
	s_cmp_lg_u32 s14, 1
	v_lshl_add_u64 v[2:3], s[10:11], 0, v[134:135]
	s_cbranch_scc1 .LBB0_465
	s_barrier
	s_setprio 1
